# prologue: -2 scale folded into cvt neg modifiers (codes stored as -e, distances and margins halved exactly)
# baseline (speedup 1.0000x reference)
.LBB0_5:
	s_or_b64 exec, exec, s[4:5]
	s_lshr_b32 s33, s3, 6
	s_lshl_b32 s3, s33, 7
	v_bfe_u32 v70, v0, 4, 2
	s_lshl_b32 s4, s2, 2
	v_or_b32_e32 v18, s3, v70
	v_lshlrev_b32_e32 v2, 4, v0
	s_and_b32 s25, s4, 28
	v_and_b32_e32 v84, 0xf0, v2
	v_or_b32_e32 v2, s25, v18
	s_add_i32 s5, s4, 4
	v_lshl_or_b32 v2, v2, 8, v84
	s_and_b32 s34, s5, 28
	s_waitcnt lgkmcnt(0)
	global_load_dwordx4 v[2:5], v2, s[22:23]
	v_or_b32_e32 v6, s34, v18
	s_add_i32 s5, s4, 8
	v_lshl_or_b32 v6, v6, 8, v84
	s_and_b32 s35, s5, 28
	global_load_dwordx4 v[6:9], v6, s[22:23]
	v_or_b32_e32 v10, s35, v18
	s_add_i32 s5, s4, 12
	v_lshl_or_b32 v10, v10, 8, v84
	s_and_b32 s36, s5, 28
	global_load_dwordx4 v[10:13], v10, s[22:23]
	v_or_b32_e32 v14, s36, v18
	v_lshl_or_b32 v14, v14, 8, v84
	s_xor_b32 s37, s25, 16
	global_load_dwordx4 v[14:17], v14, s[22:23]
	v_or_b32_e32 v19, s37, v18
	s_add_i32 s5, s4, 20
	v_lshl_or_b32 v19, v19, 8, v84
	s_and_b32 s38, s5, 28
	global_load_dwordx4 v[46:49], v19, s[22:23]
	v_or_b32_e32 v20, s38, v18
	s_add_i32 s7, s4, 24
	v_lshl_or_b32 v20, v20, 8, v84
	s_and_b32 s39, s7, 28
	global_load_dwordx4 v[50:53], v20, s[22:23]
	v_or_b32_e32 v20, s39, v18
	s_add_i32 s4, s4, 28
	v_lshl_or_b32 v20, v20, 8, v84
	s_and_b32 s40, s4, 28
	global_load_dwordx4 v[58:61], v20, s[22:23]
	v_or_b32_e32 v18, s40, v18
	v_lshl_or_b32 v18, v18, 8, v84
	global_load_dwordx4 v[62:65], v18, s[22:23]
	v_lshlrev_b32_e32 v19, 3, v0
	s_mul_i32 s6, s33, 0x1200
	v_and_b32_e32 v19, 0x78, v19
	v_or_b32_e32 v85, 32, v70
	v_or_b32_e32 v93, s6, v19
	v_or_b32_e32 v19, s3, v85
	v_bfe_u32 v184, v0, 5, 1
	v_and_b32_e32 v181, 31, v0
	s_movk_i32 s5, 0x90
	v_mov_b32_e32 v18, s6
	v_or_b32_e32 v20, s25, v19
	v_lshlrev_b32_e32 v182, 4, v184
	v_mad_u32_u24 v18, v181, s5, v18
	v_or_b32_e32 v21, s34, v19
	v_or_b32_e32 v22, s35, v19
	v_or_b32_e32 v23, s36, v19
	v_or_b32_e32 v24, s37, v19
	v_or_b32_e32 v25, s38, v19
	v_or_b32_e32 v26, s39, v19
	v_or_b32_e32 v19, s40, v19
	v_lshl_or_b32 v43, v20, 8, v84
	v_add_u32_e32 v82, v18, v182
	v_lshl_or_b32 v44, v21, 8, v84
	v_lshl_or_b32 v45, v22, 8, v84
	v_lshl_or_b32 v71, v23, 8, v84
	v_lshl_or_b32 v72, v24, 8, v84
	v_lshl_or_b32 v73, v25, 8, v84
	v_lshl_or_b32 v74, v26, 8, v84
	v_lshl_or_b32 v75, v19, 8, v84
	global_load_dwordx4 v[66:69], v43, s[22:23]
	global_load_dwordx4 v[54:57], v44, s[22:23]
	global_load_dwordx4 v[38:41], v45, s[22:23]
	global_load_dwordx4 v[34:37], v71, s[22:23]
	global_load_dwordx4 v[30:33], v72, s[22:23]
	global_load_dwordx4 v[26:29], v73, s[22:23]
	global_load_dwordx4 v[22:25], v74, s[22:23]
	global_load_dwordx4 v[18:21], v75, s[22:23]
	v_or_b32_e32 v42, s25, v70
	v_or_b32_e32 v43, s34, v70
	v_or_b32_e32 v44, s35, v70
	v_or_b32_e32 v45, s36, v70
	s_waitcnt vmcnt(15)
	v_cvt_pk_f16_f32 v2, -v2, -v3
	v_cvt_pk_f16_f32 v3, -v4, -v5
	v_mad_u32_u24 v4, v42, s5, v93
	ds_write_b64 v4, v[2:3]
	s_waitcnt vmcnt(14)
	v_cvt_pk_f16_f32 v2, -v6, -v7
	v_cvt_pk_f16_f32 v3, -v8, -v9
	v_mad_u32_u24 v4, v43, s5, v93
	ds_write_b64 v4, v[2:3]
	s_waitcnt vmcnt(13)
	v_cvt_pk_f16_f32 v2, -v10, -v11
	v_cvt_pk_f16_f32 v3, -v12, -v13
	v_mad_u32_u24 v4, v44, s5, v93
	ds_write_b64 v4, v[2:3]
	s_waitcnt vmcnt(12)
	v_cvt_pk_f16_f32 v2, -v14, -v15
	v_cvt_pk_f16_f32 v3, -v16, -v17
	v_mad_u32_u24 v4, v45, s5, v93
	ds_write_b64 v4, v[2:3]
	s_waitcnt vmcnt(11)
	v_cvt_pk_f16_f32 v2, -v46, -v47
	v_cvt_pk_f16_f32 v3, -v48, -v49
	v_bitop3_b32 v46, s25, v70, 16 bitop3:0xde
	v_mad_u32_u24 v4, v46, s5, v93
	ds_write_b64 v4, v[2:3]
	s_waitcnt vmcnt(10)
	v_cvt_pk_f16_f32 v2, -v50, -v51
	v_cvt_pk_f16_f32 v3, -v52, -v53
	v_or_b32_e32 v47, s38, v70
	v_mad_u32_u24 v4, v47, s5, v93
	ds_write_b64 v4, v[2:3]
	s_waitcnt vmcnt(9)
	v_cvt_pk_f16_f32 v2, -v58, -v59
	v_cvt_pk_f16_f32 v3, -v60, -v61
	v_or_b32_e32 v48, s39, v70
	v_mad_u32_u24 v4, v48, s5, v93
	ds_write_b64 v4, v[2:3]
	s_waitcnt vmcnt(8)
	v_cvt_pk_f16_f32 v2, -v62, -v63
	v_cvt_pk_f16_f32 v3, -v64, -v65
	v_or_b32_e32 v49, s40, v70
	v_mad_u32_u24 v4, v49, s5, v93
	ds_write_b64 v4, v[2:3]
	s_waitcnt lgkmcnt(0)
	ds_read_b128 v[98:101], v82
	ds_read_b128 v[102:105], v82 offset:32
	s_waitcnt lgkmcnt(1)
	v_mfma_f32_32x32x16_f16 v[2:17], v[98:101], v[98:101], 0
	ds_read_b128 v[106:109], v82 offset:64
	ds_read_b128 v[110:113], v82 offset:96
	s_waitcnt lgkmcnt(0)
	v_and_b32_e32 v50, 3, v0
	v_cmp_ne_u32_e64 s[6:7], 0, v50
	v_cmp_ne_u32_e64 s[4:5], 1, v50
	v_cmp_eq_u32_e32 vcc, 2, v50
	s_waitcnt lgkmcnt(2)
	v_mfma_f32_32x32x16_f16 v[2:17], v[102:105], v[102:105], v[2:17]
	s_waitcnt lgkmcnt(1)
	v_mfma_f32_32x32x16_f16 v[2:17], v[106:109], v[106:109], v[2:17]
	s_waitcnt lgkmcnt(0)
	v_mfma_f32_32x32x16_f16 v[2:17], v[110:113], v[110:113], v[2:17]
	s_and_saveexec_b64 s[8:9], s[6:7]
	s_xor_b64 s[8:9], exec, s[8:9]
	s_cbranch_execz .LBB0_9
	s_nop 8
	v_mov_b32_e32 v2, v3
	s_and_saveexec_b64 s[12:13], s[4:5]
	s_xor_b64 s[12:13], exec, s[12:13]
	v_cndmask_b32_e32 v2, v5, v4, vcc
	s_andn2_saveexec_b64 s[12:13], s[12:13]
	s_or_b64 exec, exec, s[12:13]

.LBB0_21:
	s_andn2_saveexec_b64 s[8:9], s[8:9]
	s_or_b64 exec, exec, s[8:9]
	v_mov_b32_e32 v13, 0x1e400
	v_lshl_or_b32 v13, v181, 2, v13
	v_lshrrev_b32_e32 v15, 3, v181
	v_bfe_u32 v16, v0, 2, 1
	v_mul_u32_u24_e32 v12, 0x90, v42
	v_mul_u32_u24_e32 v11, 0x90, v43
	v_mul_u32_u24_e32 v9, 0x90, v44
	v_mul_u32_u24_e32 v8, 0x90, v45
	v_mul_u32_u24_e32 v7, 0x90, v46
	v_mul_u32_u24_e32 v5, 0x90, v47
	v_mul_u32_u24_e32 v4, 0x90, v48
	v_mul_u32_u24_e32 v3, 0x90, v49
	v_cmp_eq_u32_e64 s[16:17], v184, v16
	v_cmp_gt_u32_e64 s[8:9], 8, v181
	v_cmp_eq_u32_e64 s[12:13], 1, v15
	v_cmp_eq_u32_e64 s[14:15], 2, v15
	v_lshl_add_u32 v83, s3, 2, v13
	s_and_saveexec_b64 s[28:29], s[16:17]
	v_cndmask_b32_e64 v10, v14, v10, s[14:15]
	v_cndmask_b32_e64 v6, v10, v6, s[12:13]
	v_cndmask_b32_e64 v2, v6, v2, s[8:9]
	v_mul_f32_e32 v2, 0.5, v2
	ds_write_b32 v83, v2
	s_or_b64 exec, exec, s[28:29]
	v_add3_u32 v2, v85, s3, 32
	v_or_b32_e32 v6, s25, v2
	v_lshl_or_b32 v6, v6, 8, v84
	v_or_b32_e32 v10, s34, v2
	v_lshl_or_b32 v10, v10, 8, v84
	global_load_dwordx4 v[78:81], v6, s[22:23]
	global_load_dwordx4 v[70:73], v10, s[22:23]
	v_or_b32_e32 v6, s35, v2
	v_lshl_or_b32 v6, v6, 8, v84
	v_or_b32_e32 v10, s36, v2
	v_lshl_or_b32 v10, v10, 8, v84
	global_load_dwordx4 v[74:77], v6, s[22:23]
	global_load_dwordx4 v[58:61], v10, s[22:23]
	v_or_b32_e32 v6, s37, v2
	v_lshl_or_b32 v6, v6, 8, v84
	v_or_b32_e32 v10, s38, v2
	v_lshl_or_b32 v10, v10, 8, v84
	global_load_dwordx4 v[62:65], v6, s[22:23]
	global_load_dwordx4 v[46:49], v10, s[22:23]
	v_or_b32_e32 v6, s39, v2
	v_lshl_or_b32 v6, v6, 8, v84
	v_or_b32_e32 v2, s40, v2
	v_lshl_or_b32 v2, v2, 8, v84
	global_load_dwordx4 v[50:53], v6, s[22:23]
	global_load_dwordx4 v[42:45], v2, s[22:23]
	s_waitcnt vmcnt(15)
	v_cvt_pk_f16_f32 v14, -v66, -v67
	v_cvt_pk_f16_f32 v15, -v68, -v69
	v_add_u32_e32 v86, v93, v12
	ds_write_b64 v86, v[14:15]
	s_waitcnt vmcnt(14)
	v_cvt_pk_f16_f32 v12, -v54, -v55
	v_cvt_pk_f16_f32 v13, -v56, -v57
	v_add_u32_e32 v87, v93, v11
	ds_write_b64 v87, v[12:13]
	s_waitcnt vmcnt(13)
	v_cvt_pk_f16_f32 v10, -v38, -v39
	v_cvt_pk_f16_f32 v11, -v40, -v41
	v_add_u32_e32 v88, v93, v9
	ds_write_b64 v88, v[10:11]
	s_waitcnt vmcnt(12)
	v_cvt_pk_f16_f32 v10, -v34, -v35
	v_cvt_pk_f16_f32 v11, -v36, -v37
	v_add_u32_e32 v89, v93, v8
	ds_write_b64 v89, v[10:11]
	s_waitcnt vmcnt(11)
	v_cvt_pk_f16_f32 v8, -v30, -v31
	v_cvt_pk_f16_f32 v9, -v32, -v33
	v_add_u32_e32 v90, v93, v7
	ds_write_b64 v90, v[8:9]
	s_waitcnt vmcnt(10)
	v_cvt_pk_f16_f32 v6, -v26, -v27
	v_cvt_pk_f16_f32 v7, -v28, -v29
	v_add_u32_e32 v91, v93, v5
	ds_write_b64 v91, v[6:7]
	s_waitcnt vmcnt(9)
	v_cvt_pk_f16_f32 v6, -v22, -v23
	v_cvt_pk_f16_f32 v7, -v24, -v25
	v_add_u32_e32 v92, v93, v4
	ds_write_b64 v92, v[6:7]
	s_waitcnt vmcnt(8)
	v_cvt_pk_f16_f32 v4, -v18, -v19
	v_cvt_pk_f16_f32 v5, -v20, -v21
	v_add_u32_e32 v93, v93, v3
	ds_write_b64 v93, v[4:5]
	s_waitcnt lgkmcnt(0)
	ds_read_b128 v[114:117], v82
	ds_read_b128 v[118:121], v82 offset:32
	s_waitcnt lgkmcnt(1)
	v_mfma_f32_32x32x16_f16 v[2:17], v[114:117], v[114:117], 0
	ds_read_b128 v[122:125], v82 offset:64
	ds_read_b128 v[126:129], v82 offset:96
	s_waitcnt lgkmcnt(0)
	s_waitcnt lgkmcnt(2)
	v_mfma_f32_32x32x16_f16 v[2:17], v[118:121], v[118:121], v[2:17]
	s_waitcnt lgkmcnt(1)
	v_mfma_f32_32x32x16_f16 v[2:17], v[122:125], v[122:125], v[2:17]
	s_waitcnt lgkmcnt(0)
	v_mfma_f32_32x32x16_f16 v[2:17], v[126:129], v[126:129], v[2:17]
	s_and_saveexec_b64 s[28:29], s[6:7]
	s_xor_b64 s[28:29], exec, s[28:29]
	s_cbranch_execz .LBB0_27
	s_nop 8
	v_mov_b32_e32 v2, v3
	s_and_saveexec_b64 s[30:31], s[4:5]
	s_xor_b64 s[30:31], exec, s[30:31]
	v_cndmask_b32_e32 v2, v5, v4, vcc
	s_andn2_saveexec_b64 s[30:31], s[30:31]
	s_or_b64 exec, exec, s[30:31]

.LBB0_39:
	s_andn2_saveexec_b64 s[28:29], s[28:29]
	s_or_b64 exec, exec, s[28:29]
	s_and_saveexec_b64 s[28:29], s[16:17]
	v_cndmask_b32_e64 v3, v14, v10, s[14:15]
	v_cndmask_b32_e64 v3, v3, v6, s[12:13]
	v_cndmask_b32_e64 v2, v3, v2, s[8:9]
	v_mul_f32_e32 v2, 0.5, v2
	ds_write_b32 v83, v2 offset:128
	s_or_b64 exec, exec, s[28:29]
	v_add3_u32 v2, v85, s3, 64
	v_or_b32_e32 v3, s25, v2
	v_lshl_or_b32 v3, v3, 8, v84
	v_or_b32_e32 v4, s34, v2
	v_lshl_or_b32 v4, v4, 8, v84
	global_load_dwordx4 v[66:69], v3, s[22:23]
	global_load_dwordx4 v[38:41], v4, s[22:23]
	v_or_b32_e32 v3, s35, v2
	v_lshl_or_b32 v3, v3, 8, v84
	v_or_b32_e32 v4, s36, v2
	v_lshl_or_b32 v4, v4, 8, v84
	global_load_dwordx4 v[54:57], v3, s[22:23]
	global_load_dwordx4 v[30:33], v4, s[22:23]
	v_or_b32_e32 v3, s37, v2
	v_lshl_or_b32 v3, v3, 8, v84
	v_or_b32_e32 v4, s38, v2
	v_lshl_or_b32 v4, v4, 8, v84
	global_load_dwordx4 v[34:37], v3, s[22:23]
	global_load_dwordx4 v[22:25], v4, s[22:23]
	v_or_b32_e32 v3, s39, v2
	v_lshl_or_b32 v3, v3, 8, v84
	v_or_b32_e32 v2, s40, v2
	v_lshl_or_b32 v2, v2, 8, v84
	global_load_dwordx4 v[26:29], v3, s[22:23]
	global_load_dwordx4 v[18:21], v2, s[22:23]
	s_waitcnt vmcnt(15)
	v_cvt_pk_f16_f32 v2, -v78, -v79
	v_cvt_pk_f16_f32 v3, -v80, -v81
	ds_write_b64 v86, v[2:3]
	s_waitcnt vmcnt(14)
	v_cvt_pk_f16_f32 v2, -v70, -v71
	v_cvt_pk_f16_f32 v3, -v72, -v73
	ds_write_b64 v87, v[2:3]
	s_waitcnt vmcnt(13)
	v_cvt_pk_f16_f32 v2, -v74, -v75
	v_cvt_pk_f16_f32 v3, -v76, -v77
	ds_write_b64 v88, v[2:3]
	s_waitcnt vmcnt(12)
	v_cvt_pk_f16_f32 v2, -v58, -v59
	v_cvt_pk_f16_f32 v3, -v60, -v61
	ds_write_b64 v89, v[2:3]
	s_waitcnt vmcnt(11)
	v_cvt_pk_f16_f32 v2, -v62, -v63
	v_cvt_pk_f16_f32 v3, -v64, -v65
	ds_write_b64 v90, v[2:3]
	s_waitcnt vmcnt(10)
	v_cvt_pk_f16_f32 v2, -v46, -v47
	v_cvt_pk_f16_f32 v3, -v48, -v49
	ds_write_b64 v91, v[2:3]
	s_waitcnt vmcnt(9)
	v_cvt_pk_f16_f32 v2, -v50, -v51
	v_cvt_pk_f16_f32 v3, -v52, -v53
	ds_write_b64 v92, v[2:3]
	s_waitcnt vmcnt(8)
	v_cvt_pk_f16_f32 v2, -v42, -v43
	v_cvt_pk_f16_f32 v3, -v44, -v45
	ds_write_b64 v93, v[2:3]
	s_waitcnt lgkmcnt(0)
	ds_read_b128 v[130:133], v82
	ds_read_b128 v[134:137], v82 offset:32
	s_waitcnt lgkmcnt(1)
	v_mfma_f32_32x32x16_f16 v[2:17], v[130:133], v[130:133], 0
	ds_read_b128 v[138:141], v82 offset:64
	ds_read_b128 v[142:145], v82 offset:96
	s_waitcnt lgkmcnt(0)
	s_waitcnt lgkmcnt(2)
	v_mfma_f32_32x32x16_f16 v[2:17], v[134:137], v[134:137], v[2:17]
	s_waitcnt lgkmcnt(1)
	v_mfma_f32_32x32x16_f16 v[2:17], v[138:141], v[138:141], v[2:17]
	s_waitcnt lgkmcnt(0)
	v_mfma_f32_32x32x16_f16 v[2:17], v[142:145], v[142:145], v[2:17]
	s_and_saveexec_b64 s[28:29], s[6:7]
	s_xor_b64 s[28:29], exec, s[28:29]
	s_cbranch_execz .LBB0_45
	s_nop 8
	v_mov_b32_e32 v2, v3
	s_and_saveexec_b64 s[30:31], s[4:5]
	s_xor_b64 s[30:31], exec, s[30:31]
	v_cndmask_b32_e32 v2, v5, v4, vcc
	s_andn2_saveexec_b64 s[30:31], s[30:31]
	s_or_b64 exec, exec, s[30:31]

.LBB0_57:
	s_andn2_saveexec_b64 s[28:29], s[28:29]
	s_or_b64 exec, exec, s[28:29]
	s_and_saveexec_b64 s[28:29], s[16:17]
	v_cndmask_b32_e64 v3, v14, v10, s[14:15]
	v_cndmask_b32_e64 v3, v3, v6, s[12:13]
	v_cndmask_b32_e64 v2, v3, v2, s[8:9]
	v_mul_f32_e32 v2, 0.5, v2
	ds_write_b32 v83, v2 offset:256
	s_or_b64 exec, exec, s[28:29]
	s_waitcnt vmcnt(7)
	v_cvt_pk_f16_f32 v2, -v66, -v67
	v_cvt_pk_f16_f32 v3, -v68, -v69
	ds_write_b64 v86, v[2:3]
	s_waitcnt vmcnt(6)
	v_cvt_pk_f16_f32 v2, -v38, -v39
	v_cvt_pk_f16_f32 v3, -v40, -v41
	ds_write_b64 v87, v[2:3]
	s_waitcnt vmcnt(5)
	v_cvt_pk_f16_f32 v2, -v54, -v55
	v_cvt_pk_f16_f32 v3, -v56, -v57
	ds_write_b64 v88, v[2:3]
	s_waitcnt vmcnt(4)
	v_cvt_pk_f16_f32 v2, -v30, -v31
	v_cvt_pk_f16_f32 v3, -v32, -v33
	ds_write_b64 v89, v[2:3]
	s_waitcnt vmcnt(3)
	v_cvt_pk_f16_f32 v2, -v34, -v35
	v_cvt_pk_f16_f32 v3, -v36, -v37
	ds_write_b64 v90, v[2:3]
	s_waitcnt vmcnt(2)
	v_cvt_pk_f16_f32 v2, -v22, -v23
	v_cvt_pk_f16_f32 v3, -v24, -v25
	ds_write_b64 v91, v[2:3]
	s_waitcnt vmcnt(1)
	v_cvt_pk_f16_f32 v2, -v26, -v27
	v_cvt_pk_f16_f32 v3, -v28, -v29
	ds_write_b64 v92, v[2:3]
	s_waitcnt vmcnt(0)
	v_cvt_pk_f16_f32 v2, -v18, -v19
	v_cvt_pk_f16_f32 v3, -v20, -v21
	ds_write_b64 v93, v[2:3]
	s_waitcnt lgkmcnt(0)
	ds_read_b128 v[146:149], v82
	ds_read_b128 v[150:153], v82 offset:32
	s_waitcnt lgkmcnt(1)
	v_mfma_f32_32x32x16_f16 v[2:17], v[146:149], v[146:149], 0
	ds_read_b128 v[154:157], v82 offset:64
	ds_read_b128 v[158:161], v82 offset:96
	s_waitcnt lgkmcnt(0)
	s_waitcnt lgkmcnt(2)
	v_mfma_f32_32x32x16_f16 v[2:17], v[150:153], v[150:153], v[2:17]
	s_waitcnt lgkmcnt(1)
	v_mfma_f32_32x32x16_f16 v[2:17], v[154:157], v[154:157], v[2:17]
	s_waitcnt lgkmcnt(0)
	v_mfma_f32_32x32x16_f16 v[2:17], v[158:161], v[158:161], v[2:17]
	s_and_saveexec_b64 s[28:29], s[6:7]
	s_xor_b64 s[28:29], exec, s[28:29]
	s_cbranch_execz .LBB0_63
	s_nop 8
	v_mov_b32_e32 v2, v3
	s_and_saveexec_b64 s[30:31], s[4:5]
	s_xor_b64 s[30:31], exec, s[30:31]
	v_cndmask_b32_e32 v2, v5, v4, vcc
	s_andn2_saveexec_b64 s[30:31], s[30:31]
	s_or_b64 exec, exec, s[30:31]

.LBB0_75:
	s_andn2_saveexec_b64 s[4:5], s[6:7]
	s_or_b64 exec, exec, s[4:5]
	s_and_saveexec_b64 s[4:5], s[16:17]
	v_cndmask_b32_e64 v3, v14, v10, s[14:15]
	v_cndmask_b32_e64 v3, v3, v6, s[12:13]
	v_cndmask_b32_e64 v2, v3, v2, s[8:9]
	v_mul_f32_e32 v2, 0.5, v2
	ds_write_b32 v83, v2 offset:384
	s_or_b64 exec, exec, s[4:5]
	v_lshl_or_b32 v2, s33, 9, v182
	s_waitcnt lgkmcnt(0)
	v_add_u32_e32 v62, 0x1e400, v2
	ds_read_b128 v[2:5], v62
	ds_read_b128 v[6:9], v62 offset:32
	ds_read_b128 v[10:13], v62 offset:64
	ds_read_b128 v[14:17], v62 offset:96
	ds_read_b128 v[18:21], v62 offset:128
	ds_read_b128 v[22:25], v62 offset:160
	ds_read_b128 v[26:29], v62 offset:192
	ds_read_b128 v[30:33], v62 offset:224
	ds_read_b128 v[34:37], v62 offset:256
	ds_read_b128 v[38:41], v62 offset:288
	ds_read_b128 v[42:45], v62 offset:320
	ds_read_b128 v[46:49], v62 offset:352
	ds_read_b128 v[50:53], v62 offset:384
	ds_read_b128 v[54:57], v62 offset:416
	ds_read_b128 v[58:61], v62 offset:448
	ds_read_b128 v[62:65], v62 offset:480
	v_cndmask_b32_e64 v66, 0, 1, s[26:27]
	v_mul_u32_u24_e32 v185, 0x90, v181
	v_cmp_ne_u32_e64 s[4:5], 1, v66
	s_andn2_b64 vcc, exec, s[26:27]
	v_lshlrev_b32_e32 v66, 3, v1
	v_lshlrev_b32_e32 v186, 8, v183
	s_waitcnt lgkmcnt(0)
	s_barrier
	s_cbranch_vccnz .LBB0_79
	v_and_b32_e32 v67, 0xff, v0
	v_mov_b32_e32 v72, 0x12000
	v_lshl_or_b32 v67, v67, 4, v72
	s_mov_b32 s6, 0x13000
	ds_write_b128 v67, v[174:177]
	v_or3_b32 v67, v186, v178, s6
	ds_write_b128 v67, v[170:173]
	v_or_b32_e32 v67, s24, v183
	v_or_b32_e32 v72, 64, v67
	v_ashrrev_i32_e32 v73, 31, v72
	v_or_b32_e32 v74, 0x50, v67
	v_lshlrev_b64 v[72:73], 8, v[72:73]
	v_ashrrev_i32_e32 v75, 31, v74
	v_lshl_add_u64 v[72:73], s[20:21], 0, v[72:73]
	v_mov_b32_e32 v179, 0
	v_lshlrev_b64 v[74:75], 8, v[74:75]
	v_lshl_add_u64 v[72:73], v[72:73], 0, v[178:179]
	v_lshl_add_u64 v[74:75], s[20:21], 0, v[74:75]
	v_cvt_pk_f16_f32 v69, v176, v177
	v_cvt_pk_f16_f32 v68, v174, v175
	v_cvt_pk_f16_f32 v71, v172, v173
	v_cvt_pk_f16_f32 v70, v170, v171
	v_lshl_add_u64 v[74:75], v[74:75], 0, v[178:179]
	global_load_dwordx4 v[174:177], v[72:73], off nt
	global_load_dwordx4 v[170:173], v[74:75], off nt
	s_movk_i32 s6, 0x90
	v_mad_u32_u24 v67, v183, s6, v66
	ds_write_b64 v67, v[68:69]
	ds_write_b64 v67, v[70:71] offset:2304

.LBB0_85:
	s_waitcnt vmcnt(3)
	v_mov_b32_e32 v167, 0
	s_and_b64 vcc, exec, s[0:1]
	s_cbranch_vccz .LBB0_107
	s_lshl_b32 s0, s33, 2
	s_and_b32 s0, s0, 12
	v_bfe_u32 v192, v0, 3, 2
	s_waitcnt vmcnt(0)
	v_or3_b32 v172, v192, s0, v182
	v_and_b32_e32 v170, 7, v0
	s_setprio 2
	v_mov_b32_e32 v222, 0
	v_mov_b32_e32 v223, 0
	ds_read_b128 v[162:165], v179
	ds_read_b128 v[166:169], v179 offset:32
	ds_read_b128 v[174:177], v179 offset:64
	ds_read_b128 v[188:191], v179 offset:96
	s_movk_i32 s16, 0xffc0
	s_mov_b32 s25, 0x7f61b1e6
	s_waitcnt lgkmcnt(0)
	v_mfma_f32_32x32x16_f16 v[66:81], v[98:101], v[162:165], v[2:17]
	s_lshl_b32 s1, s33, 4
	s_add_i32 s1, s1, 0x1a000
	s_mov_b32 s4, 0x1a000
	v_cmp_eq_u32_e32 vcc, 0, v170
	s_mov_b32 s17, 1
	v_add_u32_e32 v179, 0x1200, v179
	s_mov_b32 s26, 0x3d3851ec
	v_mfma_f32_32x32x16_f16 v[66:81], v[102:105], v[166:169], v[66:81]
	s_movk_i32 s27, 0x3ff
	s_movk_i32 s28, 0x3ff0
	v_mfma_f32_32x32x16_f16 v[66:81], v[106:109], v[174:177], v[66:81]
	v_mfma_f32_32x32x16_f16 v[66:81], v[110:113], v[188:191], v[66:81]
	s_nop 11
	v_and_b32_e32 v82, 0xffffffc0, v66
	v_and_or_b32 v83, v67, s16, 1
	v_and_or_b32 v84, v68, s16, 2
	v_and_or_b32 v85, v69, s16, 3
	v_and_or_b32 v86, v70, s16, 4
	v_and_or_b32 v87, v71, s16, 5
	v_and_or_b32 v88, v72, s16, 6
	v_and_or_b32 v89, v73, s16, 7
	v_and_or_b32 v90, v74, s16, 8
	v_and_or_b32 v91, v75, s16, 9
	v_and_or_b32 v92, v76, s16, 10
	v_and_or_b32 v93, v77, s16, 11
	v_and_or_b32 v94, v78, s16, 12
	v_and_or_b32 v95, v79, s16, 13
	v_and_or_b32 v96, v80, s16, 14
	v_and_or_b32 v97, v81, s16, 15
	v_mfma_f32_32x32x16_f16 v[66:81], v[114:117], v[162:165], v[18:33]
	v_med3_f32 v171, v82, v83, s25
	v_min3_f32 v82, v82, s25, v83
	v_med3_f32 v83, v82, v84, v85
	v_min3_f32 v82, v82, v84, v85
	v_med3_f32 v84, v82, v86, v87
	v_min3_f32 v82, v82, v86, v87
	v_min3_f32 v83, v171, s25, v83
	v_mfma_f32_32x32x16_f16 v[66:81], v[118:121], v[166:169], v[66:81]
	v_med3_f32 v85, v82, v88, v89
	v_min3_f32 v82, v82, v88, v89
	v_min3_f32 v83, v83, v84, v85
	v_med3_f32 v84, v82, v90, v91
	v_min3_f32 v82, v82, v90, v91
	v_med3_f32 v85, v82, v92, v93
	v_min3_f32 v82, v82, v92, v93
	v_mfma_f32_32x32x16_f16 v[66:81], v[122:125], v[174:177], v[66:81]
	v_min3_f32 v83, v83, v84, v85
	v_med3_f32 v84, v82, v94, v95
	v_min3_f32 v82, v82, v94, v95
	v_med3_f32 v85, v82, v96, v97
	v_min3_f32 v171, v82, v96, v97
	v_min3_f32 v173, v83, v84, v85
	v_mfma_f32_32x32x16_f16 v[66:81], v[126:129], v[188:191], v[66:81]
	v_mfma_f32_32x32x16_f16 v[82:97], v[130:133], v[162:165], v[34:49]
	s_nop 10
	v_and_or_b32 v66, v66, s16, 16
	v_and_or_b32 v67, v67, s16, 17
	v_and_or_b32 v68, v68, s16, 18
	v_and_or_b32 v69, v69, s16, 19
	v_med3_f32 v187, v171, v66, v67
	v_min3_f32 v66, v171, v66, v67
	v_and_or_b32 v70, v70, s16, 20
	v_and_or_b32 v71, v71, s16, 21
	v_med3_f32 v67, v66, v68, v69
	v_min3_f32 v66, v66, v68, v69
	v_and_or_b32 v72, v72, s16, 22
	v_and_or_b32 v73, v73, s16, 23
	v_med3_f32 v68, v66, v70, v71
	v_min3_f32 v66, v66, v70, v71
	v_and_or_b32 v74, v74, s16, 24
	v_and_or_b32 v75, v75, s16, 25
	v_min3_f32 v67, v173, v187, v67
	v_med3_f32 v69, v66, v72, v73
	v_min3_f32 v66, v66, v72, v73
	v_and_or_b32 v76, v76, s16, 26
	v_and_or_b32 v77, v77, s16, 27
	v_min3_f32 v67, v67, v68, v69
	v_med3_f32 v68, v66, v74, v75
	v_min3_f32 v66, v66, v74, v75
	v_and_or_b32 v78, v78, s16, 28
	v_and_or_b32 v79, v79, s16, 29
	v_med3_f32 v69, v66, v76, v77
	v_min3_f32 v66, v66, v76, v77
	v_and_or_b32 v80, v80, s16, 30
	v_and_or_b32 v81, v81, s16, 31
	v_min3_f32 v67, v67, v68, v69
	v_med3_f32 v68, v66, v78, v79
	v_min3_f32 v66, v66, v78, v79
	v_med3_f32 v69, v66, v80, v81
	v_mfma_f32_32x32x16_f16 v[82:97], v[134:137], v[166:169], v[82:97]
	v_min3_f32 v171, v66, v80, v81
	v_min3_f32 v173, v67, v68, v69
	v_mfma_f32_32x32x16_f16 v[66:81], v[146:149], v[162:165], v[50:65]
	v_mfma_f32_32x32x16_f16 v[82:97], v[138:141], v[174:177], v[82:97]
	v_mfma_f32_32x32x16_f16 v[66:81], v[150:153], v[166:169], v[66:81]
	v_mov_b32_e32 v167, 0
	v_mfma_f32_32x32x16_f16 v[82:97], v[142:145], v[188:191], v[82:97]
	v_mfma_f32_32x32x16_f16 v[66:81], v[154:157], v[174:177], v[66:81]
	s_nop 10
	v_and_or_b32 v82, v82, s16, 32
	v_and_or_b32 v83, v83, s16, 33
	v_and_or_b32 v84, v84, s16, 34
	v_and_or_b32 v85, v85, s16, 35
	v_med3_f32 v162, v171, v82, v83
	v_min3_f32 v82, v171, v82, v83
	v_and_or_b32 v86, v86, s16, 36
	v_mfma_f32_32x32x16_f16 v[66:81], v[158:161], v[188:191], v[66:81]
	v_and_or_b32 v87, v87, s16, 37
	v_med3_f32 v83, v82, v84, v85
	v_min3_f32 v82, v82, v84, v85
	v_and_or_b32 v88, v88, s16, 38
	v_and_or_b32 v89, v89, s16, 39
	v_med3_f32 v84, v82, v86, v87
	v_min3_f32 v82, v82, v86, v87
	v_and_or_b32 v90, v90, s16, 40
	v_and_or_b32 v91, v91, s16, 41
	v_min3_f32 v83, v173, v162, v83
	v_med3_f32 v85, v82, v88, v89
	v_min3_f32 v82, v82, v88, v89
	v_and_or_b32 v92, v92, s16, 42
	v_and_or_b32 v93, v93, s16, 43
	v_min3_f32 v83, v83, v84, v85
	v_med3_f32 v84, v82, v90, v91
	v_min3_f32 v82, v82, v90, v91
	v_and_or_b32 v94, v94, s16, 44
	v_and_or_b32 v95, v95, s16, 45
	v_med3_f32 v85, v82, v92, v93
	v_min3_f32 v82, v82, v92, v93
	v_and_or_b32 v96, v96, s16, 46
	v_and_or_b32 v97, v97, s16, 47
	v_min3_f32 v83, v83, v84, v85
	v_med3_f32 v84, v82, v94, v95
	v_min3_f32 v82, v82, v94, v95
	v_med3_f32 v85, v82, v96, v97
	v_min3_f32 v82, v82, v96, v97
	v_and_or_b32 v66, v66, s16, 48
	v_and_or_b32 v67, v67, s16, 49
	v_min3_f32 v83, v83, v84, v85
	v_and_or_b32 v68, v68, s16, 50
	v_and_or_b32 v69, v69, s16, 51
	v_med3_f32 v84, v82, v66, v67
	v_min3_f32 v66, v82, v66, v67
	v_and_or_b32 v70, v70, s16, 52
	v_and_or_b32 v71, v71, s16, 53
	v_med3_f32 v67, v66, v68, v69
	v_min3_f32 v66, v66, v68, v69
	v_and_or_b32 v72, v72, s16, 54
	v_and_or_b32 v73, v73, s16, 55
	v_med3_f32 v68, v66, v70, v71
	v_min3_f32 v66, v66, v70, v71
	v_and_or_b32 v74, v74, s16, 56
	v_and_or_b32 v75, v75, s16, 57
	v_min3_f32 v67, v83, v84, v67
	v_med3_f32 v69, v66, v72, v73
	v_min3_f32 v66, v66, v72, v73
	v_and_or_b32 v76, v76, s16, 58
	v_and_or_b32 v77, v77, s16, 59
	v_min3_f32 v67, v67, v68, v69
	v_med3_f32 v68, v66, v74, v75
	v_min3_f32 v66, v66, v74, v75
	v_and_or_b32 v78, v78, s16, 60
	v_and_or_b32 v79, v79, s16, 61
	v_med3_f32 v69, v66, v76, v77
	v_min3_f32 v66, v66, v76, v77
	v_and_or_b32 v80, v80, s16, 62
	v_or_b32_e32 v81, 63, v81
	v_min3_f32 v67, v67, v68, v69
	v_med3_f32 v68, v66, v78, v79
	v_min3_f32 v66, v66, v78, v79
	v_med3_f32 v69, v66, v80, v81
	v_min3_f32 v67, v67, v68, v69
	v_lshlrev_b32_e32 v68, 3, v184
	v_min3_f32 v66, v66, v80, v81
	v_add3_u32 v177, s1, v185, v68
	ds_write_b64 v177, v[66:67]
	v_mul_u32_u24_e32 v66, 0x90, v172
	v_lshlrev_b32_e32 v67, 4, v170
	v_add3_u32 v185, v67, v66, s4
	v_and_b32_e32 v66, 0xff, v0
	v_mov_b32_e32 v67, 0x12000
	v_or_b32_e32 v173, 16, v183
	s_mov_b32 s1, 0x12000
	v_lshl_or_b32 v175, v66, 4, v67
	v_lshlrev_b32_e32 v66, 8, v173
	v_or3_b32 v174, v66, v178, s1
	s_lshl_b32 s1, s2, 17
	v_or3_b32 v166, s1, v186, v178
	s_waitcnt lgkmcnt(0)
	s_barrier
	v_lshl_add_u64 v[168:169], s[12:13], 0, v[166:167]
	v_or_b32_e32 v166, 0x1000, v166
	v_lshlrev_b32_e32 v176, 7, v170
	v_lshl_add_u64 v[170:171], s[12:13], 0, v[166:167]
	v_add3_u32 v166, v182, s0, v192
	v_mov_b32_e32 v66, 0x20c00
	v_or_b32_e32 v187, 4, v176
	v_lshlrev_b32_e32 v188, 2, v183
	v_lshl_or_b32 v186, v166, 2, v66
	v_mov_b32_e32 v189, 0x21d44
	s_mov_b64 s[4:5], 0x2000
	v_bfrev_b32_e32 v190, 1
	s_branch .LBB0_88

.Low_noout:
	s_waitcnt lgkmcnt(6)
	v_lshlrev_b32_e32 v210, 1, v250
	v_lshlrev_b32_e32 v211, 1, v252
	v_and_b32_e32 v212, 0xfffffc03, v250
	v_and_b32_e32 v213, 0xfffffc03, v252
	v_and_b32_e32 v210, 0x78, v210
	v_and_b32_e32 v211, 0x78, v211
	v_or3_b32 v212, v212, v210, v176
	v_or3_b32 v213, v213, v211, v187
	v_min_f32_e32 v210, v212, v213
	v_max_f32_e32 v211, v212, v213
	v_min3_f32 v211, v251, v253, v211
	v_max_f32_dpp v212, v210, v210 quad_perm:[1,0,3,2] row_mask:0xf bank_mask:0xf
	v_min_f32_dpp v213, v210, v210 quad_perm:[1,0,3,2] row_mask:0xf bank_mask:0xf
	v_mov_b32_dpp v254, v211 quad_perm:[1,0,3,2] row_mask:0xf bank_mask:0xf
	v_min3_f32 v211, v211, v254, v212
	v_max_f32_dpp v212, v213, v213 quad_perm:[2,3,0,1] row_mask:0xf bank_mask:0xf
	v_min_f32_dpp v210, v213, v213 quad_perm:[2,3,0,1] row_mask:0xf bank_mask:0xf
	v_mov_b32_dpp v254, v211 quad_perm:[2,3,0,1] row_mask:0xf bank_mask:0xf
	v_min3_f32 v211, v211, v254, v212
	v_max_f32_dpp v212, v210, v210 row_half_mirror row_mask:0xf bank_mask:0xf
	v_min_f32_dpp v213, v210, v210 row_half_mirror row_mask:0xf bank_mask:0xf
	v_mov_b32_dpp v254, v211 row_half_mirror row_mask:0xf bank_mask:0xf
	v_min3_f32 v211, v211, v254, v212
	s_and_saveexec_b64 s[6:7], vcc
	s_cbranch_execz .Low_m_done
	v_sub_f32_e32 v212, v211, v213
	v_cmp_gt_f32_e64 s[0:1], s26, v212
	s_nop 1
	v_cndmask_b32_e64 v212, 0, v190, s[0:1]
	v_and_or_b32 v212, v213, s27, v212
	ds_write_b32 v186, v212
	s_and_b64 exec, exec, s[0:1]
	s_cbranch_execz .Low_m_done
	s_mov_b64 s[14:15], exec
	v_mbcnt_lo_u32_b32 v212, s14, 0
	v_mbcnt_hi_u32_b32 v212, s15, v212
	v_cmp_eq_u32_e64 s[0:1], 0, v212
	s_and_saveexec_b64 s[8:9], s[0:1]
	s_bcnt1_i32_b64 s0, s[14:15]
	v_mov_b32_e32 v254, s0
	ds_add_rtn_u32 v254, v189, v254
	s_or_b64 exec, exec, s[8:9]
	s_waitcnt lgkmcnt(0)
	v_readfirstlane_b32 s0, v254
	v_add_f32_e32 v213, 0x3d4ccccd, v213
	s_nop 0
	v_add_lshl_u32 v212, s0, v212, 2
	v_add_u32_e32 v254, 0x21400, v212
	v_add_u32_e32 v212, 0x20400, v212
	ds_write_b32 v254, v166
	ds_write_b32 v212, v213

.Low_b_doned:
	s_or_b64 exec, exec, s[6:7]
	v_add_f32_e32 v167, v167, v222
	v_add_f32_e32 v167, v167, v223
	ds_read_b128 v[66:69], v185 offset:4608
	s_movk_i32 s0, 0xfc03
	s_waitcnt lgkmcnt(0)
	v_lshlrev_b32_e32 v71, 1, v68
	v_lshlrev_b32_e32 v70, 1, v66
	v_and_b32_e32 v71, 0x78, v71
	v_and_b32_e32 v66, 0xfffffc03, v66
	v_and_b32_e32 v70, 0x78, v70
	v_and_or_b32 v68, v68, s0, v71
	v_or3_b32 v66, v66, v70, v176
	v_or3_b32 v68, v68, v176, 4
	v_max_f32_e32 v66, v66, v66
	v_max_f32_e32 v68, v68, v68
	v_min_f32_e32 v70, v66, v68
	v_max_f32_e32 v66, v66, v68
	v_mov_b32_e32 v68, 0
	v_min3_f32 v66, v67, v69, v66
	v_mov_b32_e32 v69, 0
	v_mov_b32_dpp v68, v70 quad_perm:[1,0,3,2] row_mask:0xf bank_mask:0xf
	v_max_f32_e32 v68, v68, v68
	v_mov_b32_dpp v69, v66 quad_perm:[1,0,3,2] row_mask:0xf bank_mask:0xf
	v_max_f32_e32 v71, v70, v68
	v_min3_f32 v66, v66, v69, v71
	v_min_f32_e32 v69, v70, v68
	v_mov_b32_e32 v68, 0
	v_mov_b32_e32 v70, 0
	v_mov_b32_e32 v67, 0
	v_mov_b32_dpp v68, v69 quad_perm:[2,3,0,1] row_mask:0xf bank_mask:0xf
	v_max_f32_e32 v71, v68, v68
	v_mov_b32_dpp v70, v66 quad_perm:[2,3,0,1] row_mask:0xf bank_mask:0xf
	v_max_f32_e32 v68, v69, v71
	v_min3_f32 v68, v66, v70, v68
	v_min_f32_e32 v66, v69, v71
	v_mov_b32_e32 v69, 0
	v_mov_b32_dpp v67, v68 row_half_mirror row_mask:0xf bank_mask:0xf
	s_nop 0
	v_mov_b32_dpp v69, v66 row_half_mirror row_mask:0xf bank_mask:0xf
	s_and_saveexec_b64 s[0:1], vcc
	s_cbranch_execz .LBB0_102
	v_max_f32_e32 v69, v69, v69
	v_max_f32_e32 v70, v66, v66
	v_min_f32_e32 v66, v70, v69
	v_max_f32_e32 v69, v70, v69
	v_min3_f32 v67, v68, v67, v69
	v_sub_f32_e32 v67, v67, v66
	s_mov_b32 s4, 0x3d3851ec
	v_bfrev_b32_e32 v68, 1
	v_cmp_gt_f32_e32 vcc, s4, v67
	s_movk_i32 s4, 0x3ff
	s_nop 0
	v_cndmask_b32_e32 v67, 0, v68, vcc
	v_mov_b32_e32 v68, 0x21380
	v_and_or_b32 v67, v66, s4, v67
	v_lshl_or_b32 v68, v172, 2, v68
	ds_write_b32 v68, v67
	s_and_b64 exec, exec, vcc
	s_cbranch_execz .LBB0_102
	s_mov_b64 s[6:7], exec
	v_mbcnt_lo_u32_b32 v67, s6, 0
	v_mbcnt_hi_u32_b32 v67, s7, v67
	v_cmp_eq_u32_e32 vcc, 0, v67
	s_and_saveexec_b64 s[4:5], vcc
	s_bcnt1_i32_b64 s6, s[6:7]
	v_mov_b32_e32 v68, 0x21d44
	v_mov_b32_e32 v69, s6
	ds_add_rtn_u32 v68, v68, v69
	s_or_b64 exec, exec, s[4:5]
	s_waitcnt lgkmcnt(0)
	v_readfirstlane_b32 s4, v68
	v_or_b32_e32 v69, 0x1e0, v172
	v_add_f32_e32 v66, 0x3d4ccccd, v66
	v_add_lshl_u32 v67, s4, v67, 2
	v_add_u32_e32 v68, 0x21400, v67
	v_add_u32_e32 v67, 0x20400, v67
	ds_write_b32 v68, v69
	ds_write_b32 v67, v66
